# radix select: passes 2-3 test each key and skip the LDS atomic when no lane matches the prefix (exact); histogram zeroed by ds_write_b128; replaces the 8-key group test
# speedup vs baseline: 1.0226x; 1.0078x over previous
; __global__ void __launch_bounds__(NWAVES * 64, 2) mega_fwd(Args args) {
;     ...
;                 for (int i2 = tid; i2 < 32 * HSTR; i2 += 512) hist[i2] = 0u;
.LBB0_662:
	v_lshlrev_b32_e32 v4, 2, v33
	v_mov_b32_e32 v172, 0
	v_mov_b32_e32 v173, 0
	v_mov_b32_e32 v174, 0
	v_mov_b32_e32 v175, 0
	ds_write_b128 v4, v[172:175]
	ds_write_b128 v4, v[172:175] offset:8192
	ds_write_b128 v4, v[172:175] offset:16384
	ds_write_b128 v4, v[172:175] offset:24576
	v_cmp_gt_u32_e32 vcc, 0x80, v33
	s_and_saveexec_b64 s[54:55], vcc
	ds_write_b32 v33, v1 offset:32768

; __global__ void __launch_bounds__(NWAVES * 64, 2) mega_fwd(Args args) {
;     ...
; #pragma unroll
;                 for (int ti = 0; ti < 4; ++ti)
; #pragma unroll
;                     for (int e = 0; e < 32; ++e) { const unsigned k = keys[ti][e];
;                         const unsigned x = ((k >> pshift) ^ prefix) & pmask; const unsigned inc = 1u - __builtin_elementwise_min(x, 1u);
;                         if (F.wave + 8 * ti < ntiles) __hip_atomic_fetch_add(hist + r32 * HSTR + ((k >> shift) & 255u), inc, __ATOMIC_RELAXED, __HIP_MEMORY_SCOPE_WORKGROUP);
;                         if ((e & 7) == 7) __builtin_amdgcn_sched_barrier(0); }
.Lrx_generic:
	s_and_b64 vcc, exec, s[78:79]
	s_cbranch_vccz .Lrx_generic2
	s_and_b64 vcc, exec, s[38:39]
	s_cbranch_vccnz .Lrx_p23_g1
	v_xor_b32_e32 v4, v181, v115
	v_cmp_gt_u32_e32 vcc, s92, v4
	s_cbranch_vccz .Lrx23_0
	v_bfe_u32 v5, v115, s62, 8
	v_cndmask_b32_e64 v4, 0, 1, vcc
	v_lshl_add_u32 v5, v5, 2, v3
	ds_add_u32 v5, v4
.Lrx23_0:
	v_xor_b32_e32 v172, v181, v116
	v_cmp_gt_u32_e32 vcc, s92, v172
	s_cbranch_vccz .Lrx23_1
	v_bfe_u32 v173, v116, s62, 8
	v_cndmask_b32_e64 v172, 0, 1, vcc
	v_lshl_add_u32 v173, v173, 2, v3
	ds_add_u32 v173, v172
.Lrx23_1:
	v_xor_b32_e32 v4, v181, v114
	v_cmp_gt_u32_e32 vcc, s92, v4
	s_cbranch_vccz .Lrx23_2
	v_bfe_u32 v5, v114, s62, 8
	v_cndmask_b32_e64 v4, 0, 1, vcc
	v_lshl_add_u32 v5, v5, 2, v3
	ds_add_u32 v5, v4
.Lrx23_2:
	v_xor_b32_e32 v172, v181, v117
	v_cmp_gt_u32_e32 vcc, s92, v172
	s_cbranch_vccz .Lrx23_3
	v_bfe_u32 v173, v117, s62, 8
	v_cndmask_b32_e64 v172, 0, 1, vcc
	v_lshl_add_u32 v173, v173, 2, v3
	ds_add_u32 v173, v172
.Lrx23_3:
	v_xor_b32_e32 v4, v181, v50
	v_cmp_gt_u32_e32 vcc, s92, v4
	s_cbranch_vccz .Lrx23_4
	v_bfe_u32 v5, v50, s62, 8
	v_cndmask_b32_e64 v4, 0, 1, vcc
	v_lshl_add_u32 v5, v5, 2, v3
	ds_add_u32 v5, v4
.Lrx23_4:
	v_xor_b32_e32 v172, v181, v51
	v_cmp_gt_u32_e32 vcc, s92, v172
	s_cbranch_vccz .Lrx23_5
	v_bfe_u32 v173, v51, s62, 8
	v_cndmask_b32_e64 v172, 0, 1, vcc
	v_lshl_add_u32 v173, v173, 2, v3
	ds_add_u32 v173, v172
.Lrx23_5:
	v_xor_b32_e32 v4, v181, v52
	v_cmp_gt_u32_e32 vcc, s92, v4
	s_cbranch_vccz .Lrx23_6
	v_bfe_u32 v5, v52, s62, 8
	v_cndmask_b32_e64 v4, 0, 1, vcc
	v_lshl_add_u32 v5, v5, 2, v3
	ds_add_u32 v5, v4
.Lrx23_6:
	v_xor_b32_e32 v172, v181, v53
	v_cmp_gt_u32_e32 vcc, s92, v172
	s_cbranch_vccz .Lrx23_7
	v_bfe_u32 v173, v53, s62, 8
	v_cndmask_b32_e64 v172, 0, 1, vcc
	v_lshl_add_u32 v173, v173, 2, v3
	ds_add_u32 v173, v172
.Lrx23_7:
.Lrx_p23_g1:
	s_and_b64 vcc, exec, s[38:39]
	s_cbranch_vccnz .Lrx_p23_g2
	v_xor_b32_e32 v4, v181, v42
	v_cmp_gt_u32_e32 vcc, s92, v4
	s_cbranch_vccz .Lrx23_8
	v_bfe_u32 v5, v42, s62, 8
	v_cndmask_b32_e64 v4, 0, 1, vcc
	v_lshl_add_u32 v5, v5, 2, v3
	ds_add_u32 v5, v4
.Lrx23_8:
	v_xor_b32_e32 v172, v181, v43
	v_cmp_gt_u32_e32 vcc, s92, v172
	s_cbranch_vccz .Lrx23_9
	v_bfe_u32 v173, v43, s62, 8
	v_cndmask_b32_e64 v172, 0, 1, vcc
	v_lshl_add_u32 v173, v173, 2, v3
	ds_add_u32 v173, v172
.Lrx23_9:
	v_xor_b32_e32 v4, v181, v44
	v_cmp_gt_u32_e32 vcc, s92, v4
	s_cbranch_vccz .Lrx23_10
	v_bfe_u32 v5, v44, s62, 8
	v_cndmask_b32_e64 v4, 0, 1, vcc
	v_lshl_add_u32 v5, v5, 2, v3
	ds_add_u32 v5, v4
.Lrx23_10:
	v_xor_b32_e32 v172, v181, v45
	v_cmp_gt_u32_e32 vcc, s92, v172
	s_cbranch_vccz .Lrx23_11
	v_bfe_u32 v173, v45, s62, 8
	v_cndmask_b32_e64 v172, 0, 1, vcc
	v_lshl_add_u32 v173, v173, 2, v3
	ds_add_u32 v173, v172
.Lrx23_11:
	v_xor_b32_e32 v4, v181, v46
	v_cmp_gt_u32_e32 vcc, s92, v4
	s_cbranch_vccz .Lrx23_12
	v_bfe_u32 v5, v46, s62, 8
	v_cndmask_b32_e64 v4, 0, 1, vcc
	v_lshl_add_u32 v5, v5, 2, v3
	ds_add_u32 v5, v4
.Lrx23_12:
	v_xor_b32_e32 v172, v181, v47
	v_cmp_gt_u32_e32 vcc, s92, v172
	s_cbranch_vccz .Lrx23_13
	v_bfe_u32 v173, v47, s62, 8
	v_cndmask_b32_e64 v172, 0, 1, vcc
	v_lshl_add_u32 v173, v173, 2, v3
	ds_add_u32 v173, v172
.Lrx23_13:
	v_xor_b32_e32 v4, v181, v48
	v_cmp_gt_u32_e32 vcc, s92, v4
	s_cbranch_vccz .Lrx23_14
	v_bfe_u32 v5, v48, s62, 8
	v_cndmask_b32_e64 v4, 0, 1, vcc
	v_lshl_add_u32 v5, v5, 2, v3
	ds_add_u32 v5, v4
.Lrx23_14:
	v_xor_b32_e32 v172, v181, v49
	v_cmp_gt_u32_e32 vcc, s92, v172
	s_cbranch_vccz .Lrx23_15
	v_bfe_u32 v173, v49, s62, 8
	v_cndmask_b32_e64 v172, 0, 1, vcc
	v_lshl_add_u32 v173, v173, 2, v3
	ds_add_u32 v173, v172
.Lrx23_15:
.Lrx_p23_g2:
	s_and_b64 vcc, exec, s[38:39]
	s_cbranch_vccnz .Lrx_p23_g3
	v_xor_b32_e32 v4, v181, v139
	v_cmp_gt_u32_e32 vcc, s92, v4
	s_cbranch_vccz .Lrx23_16
	v_bfe_u32 v5, v139, s62, 8
	v_cndmask_b32_e64 v4, 0, 1, vcc
	v_lshl_add_u32 v5, v5, 2, v3
	ds_add_u32 v5, v4
.Lrx23_16:
	v_xor_b32_e32 v172, v181, v136
	v_cmp_gt_u32_e32 vcc, s92, v172
	s_cbranch_vccz .Lrx23_17
	v_bfe_u32 v173, v136, s62, 8
	v_cndmask_b32_e64 v172, 0, 1, vcc
	v_lshl_add_u32 v173, v173, 2, v3
	ds_add_u32 v173, v172
.Lrx23_17:
	v_xor_b32_e32 v4, v181, v138
	v_cmp_gt_u32_e32 vcc, s92, v4
	s_cbranch_vccz .Lrx23_18
	v_bfe_u32 v5, v138, s62, 8
	v_cndmask_b32_e64 v4, 0, 1, vcc
	v_lshl_add_u32 v5, v5, 2, v3
	ds_add_u32 v5, v4
.Lrx23_18:
	v_xor_b32_e32 v172, v181, v134
	v_cmp_gt_u32_e32 vcc, s92, v172
	s_cbranch_vccz .Lrx23_19
	v_bfe_u32 v173, v134, s62, 8
	v_cndmask_b32_e64 v172, 0, 1, vcc
	v_lshl_add_u32 v173, v173, 2, v3
	ds_add_u32 v173, v172
.Lrx23_19:
	v_xor_b32_e32 v4, v181, v135
	v_cmp_gt_u32_e32 vcc, s92, v4
	s_cbranch_vccz .Lrx23_20
	v_bfe_u32 v5, v135, s62, 8
	v_cndmask_b32_e64 v4, 0, 1, vcc
	v_lshl_add_u32 v5, v5, 2, v3
	ds_add_u32 v5, v4
.Lrx23_20:
	v_xor_b32_e32 v172, v181, v137
	v_cmp_gt_u32_e32 vcc, s92, v172
	s_cbranch_vccz .Lrx23_21
	v_bfe_u32 v173, v137, s62, 8
	v_cndmask_b32_e64 v172, 0, 1, vcc
	v_lshl_add_u32 v173, v173, 2, v3
	ds_add_u32 v173, v172
.Lrx23_21:
	v_xor_b32_e32 v4, v181, v133
	v_cmp_gt_u32_e32 vcc, s92, v4
	s_cbranch_vccz .Lrx23_22
	v_bfe_u32 v5, v133, s62, 8
	v_cndmask_b32_e64 v4, 0, 1, vcc
	v_lshl_add_u32 v5, v5, 2, v3
	ds_add_u32 v5, v4
.Lrx23_22:
	v_xor_b32_e32 v172, v181, v131
	v_cmp_gt_u32_e32 vcc, s92, v172
	s_cbranch_vccz .Lrx23_23
	v_bfe_u32 v173, v131, s62, 8
	v_cndmask_b32_e64 v172, 0, 1, vcc
	v_lshl_add_u32 v173, v173, 2, v3
	ds_add_u32 v173, v172
.Lrx23_23:
.Lrx_p23_g3:
	s_and_b64 vcc, exec, s[38:39]
	s_cbranch_vccnz .Lrx_p23_g4
	v_xor_b32_e32 v4, v181, v132
	v_cmp_gt_u32_e32 vcc, s92, v4
	s_cbranch_vccz .Lrx23_24
	v_bfe_u32 v5, v132, s62, 8
	v_cndmask_b32_e64 v4, 0, 1, vcc
	v_lshl_add_u32 v5, v5, 2, v3
	ds_add_u32 v5, v4
; __global__ void __launch_bounds__(NWAVES * 64, 2) mega_fwd(Args args) {
;     ...
; #pragma unroll
;                 for (int ti = 0; ti < 4; ++ti)
; #pragma unroll
;                     for (int e = 0; e < 32; ++e) { const unsigned k = keys[ti][e];
;                         const unsigned x = ((k >> pshift) ^ prefix) & pmask; const unsigned inc = 1u - __builtin_elementwise_min(x, 1u);
;                         if (F.wave + 8 * ti < ntiles) __hip_atomic_fetch_add(hist + r32 * HSTR + ((k >> shift) & 255u), inc, __ATOMIC_RELAXED, __HIP_MEMORY_SCOPE_WORKGROUP);
;                         if ((e & 7) == 7) __builtin_amdgcn_sched_barrier(0); }
.Lrx23_24:
	v_xor_b32_e32 v172, v181, v127
	v_cmp_gt_u32_e32 vcc, s92, v172
	s_cbranch_vccz .Lrx23_25
	v_bfe_u32 v173, v127, s62, 8
	v_cndmask_b32_e64 v172, 0, 1, vcc
	v_lshl_add_u32 v173, v173, 2, v3
	ds_add_u32 v173, v172
.Lrx23_25:
	v_xor_b32_e32 v4, v181, v126
	v_cmp_gt_u32_e32 vcc, s92, v4
	s_cbranch_vccz .Lrx23_26
	v_bfe_u32 v5, v126, s62, 8
	v_cndmask_b32_e64 v4, 0, 1, vcc
	v_lshl_add_u32 v5, v5, 2, v3
	ds_add_u32 v5, v4
.Lrx23_26:
	v_xor_b32_e32 v172, v181, v129
	v_cmp_gt_u32_e32 vcc, s92, v172
	s_cbranch_vccz .Lrx23_27
	v_bfe_u32 v173, v129, s62, 8
	v_cndmask_b32_e64 v172, 0, 1, vcc
	v_lshl_add_u32 v173, v173, 2, v3
	ds_add_u32 v173, v172
.Lrx23_27:
	v_xor_b32_e32 v4, v181, v130
	v_cmp_gt_u32_e32 vcc, s92, v4
	s_cbranch_vccz .Lrx23_28
	v_bfe_u32 v5, v130, s62, 8
	v_cndmask_b32_e64 v4, 0, 1, vcc
	v_lshl_add_u32 v5, v5, 2, v3
	ds_add_u32 v5, v4
.Lrx23_28:
	v_xor_b32_e32 v172, v181, v128
	v_cmp_gt_u32_e32 vcc, s92, v172
	s_cbranch_vccz .Lrx23_29
	v_bfe_u32 v173, v128, s62, 8
	v_cndmask_b32_e64 v172, 0, 1, vcc
	v_lshl_add_u32 v173, v173, 2, v3
	ds_add_u32 v173, v172
.Lrx23_29:
	v_xor_b32_e32 v4, v181, v125
	v_cmp_gt_u32_e32 vcc, s92, v4
	s_cbranch_vccz .Lrx23_30
	v_bfe_u32 v5, v125, s62, 8
	v_cndmask_b32_e64 v4, 0, 1, vcc
	v_lshl_add_u32 v5, v5, 2, v3
	ds_add_u32 v5, v4
.Lrx23_30:
	v_xor_b32_e32 v172, v181, v62
	v_cmp_gt_u32_e32 vcc, s92, v172
	s_cbranch_vccz .Lrx23_31
	v_bfe_u32 v173, v62, s62, 8
	v_cndmask_b32_e64 v172, 0, 1, vcc
	v_lshl_add_u32 v173, v173, 2, v3
	ds_add_u32 v173, v172
.Lrx23_31:
.Lrx_p23_g4:
	s_and_b64 vcc, exec, s[36:37]
	s_cbranch_vccnz .Lrx_p23_g5
	v_xor_b32_e32 v4, v181, v119
	v_cmp_gt_u32_e32 vcc, s92, v4
	s_cbranch_vccz .Lrx23_32
	v_bfe_u32 v5, v119, s62, 8
	v_cndmask_b32_e64 v4, 0, 1, vcc
	v_lshl_add_u32 v5, v5, 2, v3
	ds_add_u32 v5, v4
.Lrx23_32:
	v_xor_b32_e32 v172, v181, v120
	v_cmp_gt_u32_e32 vcc, s92, v172
	s_cbranch_vccz .Lrx23_33
	v_bfe_u32 v173, v120, s62, 8
	v_cndmask_b32_e64 v172, 0, 1, vcc
	v_lshl_add_u32 v173, v173, 2, v3
	ds_add_u32 v173, v172
.Lrx23_33:
	v_xor_b32_e32 v4, v181, v118
	v_cmp_gt_u32_e32 vcc, s92, v4
	s_cbranch_vccz .Lrx23_34
	v_bfe_u32 v5, v118, s62, 8
	v_cndmask_b32_e64 v4, 0, 1, vcc
	v_lshl_add_u32 v5, v5, 2, v3
	ds_add_u32 v5, v4
.Lrx23_34:
	v_xor_b32_e32 v172, v181, v121
	v_cmp_gt_u32_e32 vcc, s92, v172
	s_cbranch_vccz .Lrx23_35
	v_bfe_u32 v173, v121, s62, 8
	v_cndmask_b32_e64 v172, 0, 1, vcc
	v_lshl_add_u32 v173, v173, 2, v3
	ds_add_u32 v173, v172
.Lrx23_35:
	v_xor_b32_e32 v4, v181, v82
	v_cmp_gt_u32_e32 vcc, s92, v4
	s_cbranch_vccz .Lrx23_36
	v_bfe_u32 v5, v82, s62, 8
	v_cndmask_b32_e64 v4, 0, 1, vcc
	v_lshl_add_u32 v5, v5, 2, v3
	ds_add_u32 v5, v4
.Lrx23_36:
	v_xor_b32_e32 v172, v181, v83
	v_cmp_gt_u32_e32 vcc, s92, v172
	s_cbranch_vccz .Lrx23_37
	v_bfe_u32 v173, v83, s62, 8
	v_cndmask_b32_e64 v172, 0, 1, vcc
	v_lshl_add_u32 v173, v173, 2, v3
	ds_add_u32 v173, v172
.Lrx23_37:
	v_xor_b32_e32 v4, v181, v84
	v_cmp_gt_u32_e32 vcc, s92, v4
	s_cbranch_vccz .Lrx23_38
	v_bfe_u32 v5, v84, s62, 8
	v_cndmask_b32_e64 v4, 0, 1, vcc
	v_lshl_add_u32 v5, v5, 2, v3
	ds_add_u32 v5, v4
.Lrx23_38:
	v_xor_b32_e32 v172, v181, v85
	v_cmp_gt_u32_e32 vcc, s92, v172
	s_cbranch_vccz .Lrx23_39
	v_bfe_u32 v173, v85, s62, 8
	v_cndmask_b32_e64 v172, 0, 1, vcc
	v_lshl_add_u32 v173, v173, 2, v3
	ds_add_u32 v173, v172
.Lrx23_39:
.Lrx_p23_g5:
	s_and_b64 vcc, exec, s[36:37]
	s_cbranch_vccnz .Lrx_p23_g6
	v_xor_b32_e32 v4, v181, v74
	v_cmp_gt_u32_e32 vcc, s92, v4
	s_cbranch_vccz .Lrx23_40
	v_bfe_u32 v5, v74, s62, 8
	v_cndmask_b32_e64 v4, 0, 1, vcc
	v_lshl_add_u32 v5, v5, 2, v3
	ds_add_u32 v5, v4
.Lrx23_40:
	v_xor_b32_e32 v172, v181, v75
	v_cmp_gt_u32_e32 vcc, s92, v172
	s_cbranch_vccz .Lrx23_41
	v_bfe_u32 v173, v75, s62, 8
	v_cndmask_b32_e64 v172, 0, 1, vcc
	v_lshl_add_u32 v173, v173, 2, v3
	ds_add_u32 v173, v172
.Lrx23_41:
	v_xor_b32_e32 v4, v181, v76
	v_cmp_gt_u32_e32 vcc, s92, v4
	s_cbranch_vccz .Lrx23_42
	v_bfe_u32 v5, v76, s62, 8
	v_cndmask_b32_e64 v4, 0, 1, vcc
	v_lshl_add_u32 v5, v5, 2, v3
	ds_add_u32 v5, v4
.Lrx23_42:
	v_xor_b32_e32 v172, v181, v77
	v_cmp_gt_u32_e32 vcc, s92, v172
	s_cbranch_vccz .Lrx23_43
	v_bfe_u32 v173, v77, s62, 8
	v_cndmask_b32_e64 v172, 0, 1, vcc
	v_lshl_add_u32 v173, v173, 2, v3
	ds_add_u32 v173, v172
.Lrx23_43:
	v_xor_b32_e32 v4, v181, v78
	v_cmp_gt_u32_e32 vcc, s92, v4
	s_cbranch_vccz .Lrx23_44
	v_bfe_u32 v5, v78, s62, 8
	v_cndmask_b32_e64 v4, 0, 1, vcc
	v_lshl_add_u32 v5, v5, 2, v3
	ds_add_u32 v5, v4
.Lrx23_44:
	v_xor_b32_e32 v172, v181, v79
	v_cmp_gt_u32_e32 vcc, s92, v172
	s_cbranch_vccz .Lrx23_45
	v_bfe_u32 v173, v79, s62, 8
	v_cndmask_b32_e64 v172, 0, 1, vcc
	v_lshl_add_u32 v173, v173, 2, v3
	ds_add_u32 v173, v172
.Lrx23_45:
	v_xor_b32_e32 v4, v181, v80
	v_cmp_gt_u32_e32 vcc, s92, v4
	s_cbranch_vccz .Lrx23_46
	v_bfe_u32 v5, v80, s62, 8
	v_cndmask_b32_e64 v4, 0, 1, vcc
	v_lshl_add_u32 v5, v5, 2, v3
	ds_add_u32 v5, v4
.Lrx23_46:
	v_xor_b32_e32 v172, v181, v81
	v_cmp_gt_u32_e32 vcc, s92, v172
	s_cbranch_vccz .Lrx23_47
	v_bfe_u32 v173, v81, s62, 8
	v_cndmask_b32_e64 v172, 0, 1, vcc
	v_lshl_add_u32 v173, v173, 2, v3
	ds_add_u32 v173, v172
.Lrx23_47:
.Lrx_p23_g6:
	s_and_b64 vcc, exec, s[36:37]
	s_cbranch_vccnz .Lrx_p23_g7
	v_xor_b32_e32 v4, v181, v156
	v_cmp_gt_u32_e32 vcc, s92, v4
	s_cbranch_vccz .Lrx23_48
	v_bfe_u32 v5, v156, s62, 8
	v_cndmask_b32_e64 v4, 0, 1, vcc
	v_lshl_add_u32 v5, v5, 2, v3
	ds_add_u32 v5, v4
.Lrx23_48:
	v_xor_b32_e32 v172, v181, v153
	v_cmp_gt_u32_e32 vcc, s92, v172
	s_cbranch_vccz .Lrx23_49
	v_bfe_u32 v173, v153, s62, 8
	v_cndmask_b32_e64 v172, 0, 1, vcc
	v_lshl_add_u32 v173, v173, 2, v3
	ds_add_u32 v173, v172
; __global__ void __launch_bounds__(NWAVES * 64, 2) mega_fwd(Args args) {
;     ...
; #pragma unroll
;                 for (int ti = 0; ti < 4; ++ti)
; #pragma unroll
;                     for (int e = 0; e < 32; ++e) { const unsigned k = keys[ti][e];
;                         const unsigned x = ((k >> pshift) ^ prefix) & pmask; const unsigned inc = 1u - __builtin_elementwise_min(x, 1u);
;                         if (F.wave + 8 * ti < ntiles) __hip_atomic_fetch_add(hist + r32 * HSTR + ((k >> shift) & 255u), inc, __ATOMIC_RELAXED, __HIP_MEMORY_SCOPE_WORKGROUP);
;                         if ((e & 7) == 7) __builtin_amdgcn_sched_barrier(0); }
.Lrx23_49:
	v_xor_b32_e32 v4, v181, v155
	v_cmp_gt_u32_e32 vcc, s92, v4
	s_cbranch_vccz .Lrx23_50
	v_bfe_u32 v5, v155, s62, 8
	v_cndmask_b32_e64 v4, 0, 1, vcc
	v_lshl_add_u32 v5, v5, 2, v3
	ds_add_u32 v5, v4
.Lrx23_50:
	v_xor_b32_e32 v172, v181, v151
	v_cmp_gt_u32_e32 vcc, s92, v172
	s_cbranch_vccz .Lrx23_51
	v_bfe_u32 v173, v151, s62, 8
	v_cndmask_b32_e64 v172, 0, 1, vcc
	v_lshl_add_u32 v173, v173, 2, v3
	ds_add_u32 v173, v172
.Lrx23_51:
	v_xor_b32_e32 v4, v181, v152
	v_cmp_gt_u32_e32 vcc, s92, v4
	s_cbranch_vccz .Lrx23_52
	v_bfe_u32 v5, v152, s62, 8
	v_cndmask_b32_e64 v4, 0, 1, vcc
	v_lshl_add_u32 v5, v5, 2, v3
	ds_add_u32 v5, v4
.Lrx23_52:
	v_xor_b32_e32 v172, v181, v154
	v_cmp_gt_u32_e32 vcc, s92, v172
	s_cbranch_vccz .Lrx23_53
	v_bfe_u32 v173, v154, s62, 8
	v_cndmask_b32_e64 v172, 0, 1, vcc
	v_lshl_add_u32 v173, v173, 2, v3
	ds_add_u32 v173, v172
.Lrx23_53:
	v_xor_b32_e32 v4, v181, v150
	v_cmp_gt_u32_e32 vcc, s92, v4
	s_cbranch_vccz .Lrx23_54
	v_bfe_u32 v5, v150, s62, 8
	v_cndmask_b32_e64 v4, 0, 1, vcc
	v_lshl_add_u32 v5, v5, 2, v3
	ds_add_u32 v5, v4
.Lrx23_54:
	v_xor_b32_e32 v172, v181, v148
	v_cmp_gt_u32_e32 vcc, s92, v172
	s_cbranch_vccz .Lrx23_55
	v_bfe_u32 v173, v148, s62, 8
	v_cndmask_b32_e64 v172, 0, 1, vcc
	v_lshl_add_u32 v173, v173, 2, v3
	ds_add_u32 v173, v172
.Lrx23_55:
.Lrx_p23_g7:
	s_and_b64 vcc, exec, s[36:37]
	s_cbranch_vccnz .Lrx_p23_g8
	v_xor_b32_e32 v4, v181, v149
	v_cmp_gt_u32_e32 vcc, s92, v4
	s_cbranch_vccz .Lrx23_56
	v_bfe_u32 v5, v149, s62, 8
	v_cndmask_b32_e64 v4, 0, 1, vcc
	v_lshl_add_u32 v5, v5, 2, v3
	ds_add_u32 v5, v4
.Lrx23_56:
	v_xor_b32_e32 v172, v181, v144
	v_cmp_gt_u32_e32 vcc, s92, v172
	s_cbranch_vccz .Lrx23_57
	v_bfe_u32 v173, v144, s62, 8
	v_cndmask_b32_e64 v172, 0, 1, vcc
	v_lshl_add_u32 v173, v173, 2, v3
	ds_add_u32 v173, v172
.Lrx23_57:
	v_xor_b32_e32 v4, v181, v143
	v_cmp_gt_u32_e32 vcc, s92, v4
	s_cbranch_vccz .Lrx23_58
	v_bfe_u32 v5, v143, s62, 8
	v_cndmask_b32_e64 v4, 0, 1, vcc
	v_lshl_add_u32 v5, v5, 2, v3
	ds_add_u32 v5, v4
.Lrx23_58:
	v_xor_b32_e32 v172, v181, v146
	v_cmp_gt_u32_e32 vcc, s92, v172
	s_cbranch_vccz .Lrx23_59
	v_bfe_u32 v173, v146, s62, 8
	v_cndmask_b32_e64 v172, 0, 1, vcc
	v_lshl_add_u32 v173, v173, 2, v3
	ds_add_u32 v173, v172
.Lrx23_59:
	v_xor_b32_e32 v4, v181, v147
	v_cmp_gt_u32_e32 vcc, s92, v4
	s_cbranch_vccz .Lrx23_60
	v_bfe_u32 v5, v147, s62, 8
	v_cndmask_b32_e64 v4, 0, 1, vcc
	v_lshl_add_u32 v5, v5, 2, v3
	ds_add_u32 v5, v4
.Lrx23_60:
	v_xor_b32_e32 v172, v181, v145
	v_cmp_gt_u32_e32 vcc, s92, v172
	s_cbranch_vccz .Lrx23_61
	v_bfe_u32 v173, v145, s62, 8
	v_cndmask_b32_e64 v172, 0, 1, vcc
	v_lshl_add_u32 v173, v173, 2, v3
	ds_add_u32 v173, v172
.Lrx23_61:
	v_xor_b32_e32 v4, v181, v63
	v_cmp_gt_u32_e32 vcc, s92, v4
	s_cbranch_vccz .Lrx23_62
	v_bfe_u32 v5, v63, s62, 8
	v_cndmask_b32_e64 v4, 0, 1, vcc
	v_lshl_add_u32 v5, v5, 2, v3
	ds_add_u32 v5, v4
.Lrx23_62:
	v_xor_b32_e32 v172, v181, v94
	v_cmp_gt_u32_e32 vcc, s92, v172
	s_cbranch_vccz .Lrx23_63
	v_bfe_u32 v173, v94, s62, 8
	v_cndmask_b32_e64 v172, 0, 1, vcc
	v_lshl_add_u32 v173, v173, 2, v3
	ds_add_u32 v173, v172
.Lrx23_63:
.Lrx_p23_g8:
	s_and_b64 vcc, exec, s[34:35]
	s_cbranch_vccnz .Lrx_p23_g9
	v_xor_b32_e32 v4, v181, v109
	v_cmp_gt_u32_e32 vcc, s92, v4
	s_cbranch_vccz .Lrx23_64
	v_bfe_u32 v5, v109, s62, 8
	v_cndmask_b32_e64 v4, 0, 1, vcc
	v_lshl_add_u32 v5, v5, 2, v3
	ds_add_u32 v5, v4
.Lrx23_64:
	v_xor_b32_e32 v172, v181, v122
	v_cmp_gt_u32_e32 vcc, s92, v172
	s_cbranch_vccz .Lrx23_65
	v_bfe_u32 v173, v122, s62, 8
	v_cndmask_b32_e64 v172, 0, 1, vcc
	v_lshl_add_u32 v173, v173, 2, v3
	ds_add_u32 v173, v172
.Lrx23_65:
	v_xor_b32_e32 v4, v181, v108
	v_cmp_gt_u32_e32 vcc, s92, v4
	s_cbranch_vccz .Lrx23_66
	v_bfe_u32 v5, v108, s62, 8
	v_cndmask_b32_e64 v4, 0, 1, vcc
	v_lshl_add_u32 v5, v5, 2, v3
	ds_add_u32 v5, v4
.Lrx23_66:
	v_xor_b32_e32 v172, v181, v123
	v_cmp_gt_u32_e32 vcc, s92, v172
	s_cbranch_vccz .Lrx23_67
	v_bfe_u32 v173, v123, s62, 8
	v_cndmask_b32_e64 v172, 0, 1, vcc
	v_lshl_add_u32 v173, v173, 2, v3
	ds_add_u32 v173, v172
.Lrx23_67:
	v_xor_b32_e32 v4, v181, v96
	v_cmp_gt_u32_e32 vcc, s92, v4
	s_cbranch_vccz .Lrx23_68
	v_bfe_u32 v5, v96, s62, 8
	v_cndmask_b32_e64 v4, 0, 1, vcc
	v_lshl_add_u32 v5, v5, 2, v3
	ds_add_u32 v5, v4
.Lrx23_68:
	v_xor_b32_e32 v172, v181, v97
	v_cmp_gt_u32_e32 vcc, s92, v172
	s_cbranch_vccz .Lrx23_69
	v_bfe_u32 v173, v97, s62, 8
	v_cndmask_b32_e64 v172, 0, 1, vcc
	v_lshl_add_u32 v173, v173, 2, v3
	ds_add_u32 v173, v172
.Lrx23_69:
	v_xor_b32_e32 v4, v181, v98
	v_cmp_gt_u32_e32 vcc, s92, v4
	s_cbranch_vccz .Lrx23_70
	v_bfe_u32 v5, v98, s62, 8
	v_cndmask_b32_e64 v4, 0, 1, vcc
	v_lshl_add_u32 v5, v5, 2, v3
	ds_add_u32 v5, v4
.Lrx23_70:
	v_xor_b32_e32 v172, v181, v99
	v_cmp_gt_u32_e32 vcc, s92, v172
	s_cbranch_vccz .Lrx23_71
	v_bfe_u32 v173, v99, s62, 8
	v_cndmask_b32_e64 v172, 0, 1, vcc
	v_lshl_add_u32 v173, v173, 2, v3
	ds_add_u32 v173, v172
.Lrx23_71:
.Lrx_p23_g9:
	s_and_b64 vcc, exec, s[34:35]
	s_cbranch_vccnz .Lrx_p23_g10
	v_xor_b32_e32 v4, v181, v86
	v_cmp_gt_u32_e32 vcc, s92, v4
	s_cbranch_vccz .Lrx23_72
	v_bfe_u32 v5, v86, s62, 8
	v_cndmask_b32_e64 v4, 0, 1, vcc
	v_lshl_add_u32 v5, v5, 2, v3
	ds_add_u32 v5, v4
.Lrx23_72:
	v_xor_b32_e32 v172, v181, v87
	v_cmp_gt_u32_e32 vcc, s92, v172
	s_cbranch_vccz .Lrx23_73
	v_bfe_u32 v173, v87, s62, 8
	v_cndmask_b32_e64 v172, 0, 1, vcc
	v_lshl_add_u32 v173, v173, 2, v3
	ds_add_u32 v173, v172
.Lrx23_73:
	v_xor_b32_e32 v4, v181, v88
	v_cmp_gt_u32_e32 vcc, s92, v4
	s_cbranch_vccz .Lrx23_74
	v_bfe_u32 v5, v88, s62, 8
	v_cndmask_b32_e64 v4, 0, 1, vcc
	v_lshl_add_u32 v5, v5, 2, v3
	ds_add_u32 v5, v4
; __global__ void __launch_bounds__(NWAVES * 64, 2) mega_fwd(Args args) {
;     ...
; #pragma unroll
;                 for (int ti = 0; ti < 4; ++ti)
; #pragma unroll
;                     for (int e = 0; e < 32; ++e) { const unsigned k = keys[ti][e];
;                         const unsigned x = ((k >> pshift) ^ prefix) & pmask; const unsigned inc = 1u - __builtin_elementwise_min(x, 1u);
;                         if (F.wave + 8 * ti < ntiles) __hip_atomic_fetch_add(hist + r32 * HSTR + ((k >> shift) & 255u), inc, __ATOMIC_RELAXED, __HIP_MEMORY_SCOPE_WORKGROUP);
;                         if ((e & 7) == 7) __builtin_amdgcn_sched_barrier(0); }
.Lrx23_74:
	v_xor_b32_e32 v172, v181, v89
	v_cmp_gt_u32_e32 vcc, s92, v172
	s_cbranch_vccz .Lrx23_75
	v_bfe_u32 v173, v89, s62, 8
	v_cndmask_b32_e64 v172, 0, 1, vcc
	v_lshl_add_u32 v173, v173, 2, v3
	ds_add_u32 v173, v172
.Lrx23_75:
	v_xor_b32_e32 v4, v181, v90
	v_cmp_gt_u32_e32 vcc, s92, v4
	s_cbranch_vccz .Lrx23_76
	v_bfe_u32 v5, v90, s62, 8
	v_cndmask_b32_e64 v4, 0, 1, vcc
	v_lshl_add_u32 v5, v5, 2, v3
	ds_add_u32 v5, v4
.Lrx23_76:
	v_xor_b32_e32 v172, v181, v91
	v_cmp_gt_u32_e32 vcc, s92, v172
	s_cbranch_vccz .Lrx23_77
	v_bfe_u32 v173, v91, s62, 8
	v_cndmask_b32_e64 v172, 0, 1, vcc
	v_lshl_add_u32 v173, v173, 2, v3
	ds_add_u32 v173, v172
.Lrx23_77:
	v_xor_b32_e32 v4, v181, v92
	v_cmp_gt_u32_e32 vcc, s92, v4
	s_cbranch_vccz .Lrx23_78
	v_bfe_u32 v5, v92, s62, 8
	v_cndmask_b32_e64 v4, 0, 1, vcc
	v_lshl_add_u32 v5, v5, 2, v3
	ds_add_u32 v5, v4
.Lrx23_78:
	v_xor_b32_e32 v172, v181, v93
	v_cmp_gt_u32_e32 vcc, s92, v172
	s_cbranch_vccz .Lrx23_79
	v_bfe_u32 v173, v93, s62, 8
	v_cndmask_b32_e64 v172, 0, 1, vcc
	v_lshl_add_u32 v173, v173, 2, v3
	ds_add_u32 v173, v172
.Lrx23_79:
.Lrx_p23_g10:
	s_and_b64 vcc, exec, s[34:35]
	s_cbranch_vccnz .Lrx_p23_g11
	v_xor_b32_e32 v4, v181, v170
	v_cmp_gt_u32_e32 vcc, s92, v4
	s_cbranch_vccz .Lrx23_80
	v_bfe_u32 v5, v170, s62, 8
	v_cndmask_b32_e64 v4, 0, 1, vcc
	v_lshl_add_u32 v5, v5, 2, v3
	ds_add_u32 v5, v4
.Lrx23_80:
	v_xor_b32_e32 v172, v181, v167
	v_cmp_gt_u32_e32 vcc, s92, v172
	s_cbranch_vccz .Lrx23_81
	v_bfe_u32 v173, v167, s62, 8
	v_cndmask_b32_e64 v172, 0, 1, vcc
	v_lshl_add_u32 v173, v173, 2, v3
	ds_add_u32 v173, v172
.Lrx23_81:
	v_xor_b32_e32 v4, v181, v169
	v_cmp_gt_u32_e32 vcc, s92, v4
	s_cbranch_vccz .Lrx23_82
	v_bfe_u32 v5, v169, s62, 8
	v_cndmask_b32_e64 v4, 0, 1, vcc
	v_lshl_add_u32 v5, v5, 2, v3
	ds_add_u32 v5, v4
.Lrx23_82:
	v_xor_b32_e32 v172, v181, v165
	v_cmp_gt_u32_e32 vcc, s92, v172
	s_cbranch_vccz .Lrx23_83
	v_bfe_u32 v173, v165, s62, 8
	v_cndmask_b32_e64 v172, 0, 1, vcc
	v_lshl_add_u32 v173, v173, 2, v3
	ds_add_u32 v173, v172
.Lrx23_83:
	v_xor_b32_e32 v4, v181, v166
	v_cmp_gt_u32_e32 vcc, s92, v4
	s_cbranch_vccz .Lrx23_84
	v_bfe_u32 v5, v166, s62, 8
	v_cndmask_b32_e64 v4, 0, 1, vcc
	v_lshl_add_u32 v5, v5, 2, v3
	ds_add_u32 v5, v4
.Lrx23_84:
	v_xor_b32_e32 v172, v181, v168
	v_cmp_gt_u32_e32 vcc, s92, v172
	s_cbranch_vccz .Lrx23_85
	v_bfe_u32 v173, v168, s62, 8
	v_cndmask_b32_e64 v172, 0, 1, vcc
	v_lshl_add_u32 v173, v173, 2, v3
	ds_add_u32 v173, v172
.Lrx23_85:
	v_xor_b32_e32 v4, v181, v164
	v_cmp_gt_u32_e32 vcc, s92, v4
	s_cbranch_vccz .Lrx23_86
	v_bfe_u32 v5, v164, s62, 8
	v_cndmask_b32_e64 v4, 0, 1, vcc
	v_lshl_add_u32 v5, v5, 2, v3
	ds_add_u32 v5, v4
.Lrx23_86:
	v_xor_b32_e32 v172, v181, v162
	v_cmp_gt_u32_e32 vcc, s92, v172
	s_cbranch_vccz .Lrx23_87
	v_bfe_u32 v173, v162, s62, 8
	v_cndmask_b32_e64 v172, 0, 1, vcc
	v_lshl_add_u32 v173, v173, 2, v3
	ds_add_u32 v173, v172
.Lrx23_87:
.Lrx_p23_g11:
	s_and_b64 vcc, exec, s[34:35]
	s_cbranch_vccnz .Lrx_p23_g12
	v_xor_b32_e32 v4, v181, v163
	v_cmp_gt_u32_e32 vcc, s92, v4
	s_cbranch_vccz .Lrx23_88
	v_bfe_u32 v5, v163, s62, 8
	v_cndmask_b32_e64 v4, 0, 1, vcc
	v_lshl_add_u32 v5, v5, 2, v3
	ds_add_u32 v5, v4
.Lrx23_88:
	v_xor_b32_e32 v172, v181, v158
	v_cmp_gt_u32_e32 vcc, s92, v172
	s_cbranch_vccz .Lrx23_89
	v_bfe_u32 v173, v158, s62, 8
	v_cndmask_b32_e64 v172, 0, 1, vcc
	v_lshl_add_u32 v173, v173, 2, v3
	ds_add_u32 v173, v172
.Lrx23_89:
	v_xor_b32_e32 v4, v181, v157
	v_cmp_gt_u32_e32 vcc, s92, v4
	s_cbranch_vccz .Lrx23_90
	v_bfe_u32 v5, v157, s62, 8
	v_cndmask_b32_e64 v4, 0, 1, vcc
	v_lshl_add_u32 v5, v5, 2, v3
	ds_add_u32 v5, v4
.Lrx23_90:
	v_xor_b32_e32 v172, v181, v160
	v_cmp_gt_u32_e32 vcc, s92, v172
	s_cbranch_vccz .Lrx23_91
	v_bfe_u32 v173, v160, s62, 8
	v_cndmask_b32_e64 v172, 0, 1, vcc
	v_lshl_add_u32 v173, v173, 2, v3
	ds_add_u32 v173, v172
.Lrx23_91:
	v_xor_b32_e32 v4, v181, v161
	v_cmp_gt_u32_e32 vcc, s92, v4
	s_cbranch_vccz .Lrx23_92
	v_bfe_u32 v5, v161, s62, 8
	v_cndmask_b32_e64 v4, 0, 1, vcc
	v_lshl_add_u32 v5, v5, 2, v3
	ds_add_u32 v5, v4
.Lrx23_92:
	v_xor_b32_e32 v172, v181, v159
	v_cmp_gt_u32_e32 vcc, s92, v172
	s_cbranch_vccz .Lrx23_93
	v_bfe_u32 v173, v159, s62, 8
	v_cndmask_b32_e64 v172, 0, 1, vcc
	v_lshl_add_u32 v173, v173, 2, v3
	ds_add_u32 v173, v172
.Lrx23_93:
	v_xor_b32_e32 v4, v181, v95
	v_cmp_gt_u32_e32 vcc, s92, v4
	s_cbranch_vccz .Lrx23_94
	v_bfe_u32 v5, v95, s62, 8
	v_cndmask_b32_e64 v4, 0, 1, vcc
	v_lshl_add_u32 v5, v5, 2, v3
	ds_add_u32 v5, v4
.Lrx23_94:
	v_xor_b32_e32 v172, v181, v64
	v_cmp_gt_u32_e32 vcc, s92, v172
	s_cbranch_vccz .Lrx23_95
	v_bfe_u32 v173, v64, s62, 8
	v_cndmask_b32_e64 v172, 0, 1, vcc
	v_lshl_add_u32 v173, v173, 2, v3
	ds_add_u32 v173, v172
.Lrx23_95:
.Lrx_p23_g12:
	s_and_b64 vcc, exec, s[30:31]
	s_cbranch_vccnz .Lrx_p23_g13
	v_xor_b32_e32 v4, v181, v105
	v_cmp_gt_u32_e32 vcc, s92, v4
	s_cbranch_vccz .Lrx23_96
	v_bfe_u32 v5, v105, s62, 8
	v_cndmask_b32_e64 v4, 0, 1, vcc
	v_lshl_add_u32 v5, v5, 2, v3
	ds_add_u32 v5, v4
.Lrx23_96:
	v_xor_b32_e32 v172, v181, v106
	v_cmp_gt_u32_e32 vcc, s92, v172
	s_cbranch_vccz .Lrx23_97
	v_bfe_u32 v173, v106, s62, 8
	v_cndmask_b32_e64 v172, 0, 1, vcc
	v_lshl_add_u32 v173, v173, 2, v3
	ds_add_u32 v173, v172
.Lrx23_97:
	v_xor_b32_e32 v4, v181, v104
	v_cmp_gt_u32_e32 vcc, s92, v4
	s_cbranch_vccz .Lrx23_98
	v_bfe_u32 v5, v104, s62, 8
	v_cndmask_b32_e64 v4, 0, 1, vcc
	v_lshl_add_u32 v5, v5, 2, v3
	ds_add_u32 v5, v4
.Lrx23_98:
	v_xor_b32_e32 v172, v181, v107
	v_cmp_gt_u32_e32 vcc, s92, v172
	s_cbranch_vccz .Lrx23_99
	v_bfe_u32 v173, v107, s62, 8
	v_cndmask_b32_e64 v172, 0, 1, vcc
	v_lshl_add_u32 v173, v173, 2, v3
	ds_add_u32 v173, v172
; __global__ void __launch_bounds__(NWAVES * 64, 2) mega_fwd(Args args) {
;     ...
; #pragma unroll
;                 for (int ti = 0; ti < 4; ++ti)
; #pragma unroll
;                     for (int e = 0; e < 32; ++e) { const unsigned k = keys[ti][e];
;                         const unsigned x = ((k >> pshift) ^ prefix) & pmask; const unsigned inc = 1u - __builtin_elementwise_min(x, 1u);
;                         if (F.wave + 8 * ti < ntiles) __hip_atomic_fetch_add(hist + r32 * HSTR + ((k >> shift) & 255u), inc, __ATOMIC_RELAXED, __HIP_MEMORY_SCOPE_WORKGROUP);
;                         if ((e & 7) == 7) __builtin_amdgcn_sched_barrier(0); }
.Lrx23_99:
	v_xor_b32_e32 v4, v181, v66
	v_cmp_gt_u32_e32 vcc, s92, v4
	s_cbranch_vccz .Lrx23_100
	v_bfe_u32 v5, v66, s62, 8
	v_cndmask_b32_e64 v4, 0, 1, vcc
	v_lshl_add_u32 v5, v5, 2, v3
	ds_add_u32 v5, v4
.Lrx23_100:
	v_xor_b32_e32 v172, v181, v67
	v_cmp_gt_u32_e32 vcc, s92, v172
	s_cbranch_vccz .Lrx23_101
	v_bfe_u32 v173, v67, s62, 8
	v_cndmask_b32_e64 v172, 0, 1, vcc
	v_lshl_add_u32 v173, v173, 2, v3
	ds_add_u32 v173, v172
.Lrx23_101:
	v_xor_b32_e32 v4, v181, v68
	v_cmp_gt_u32_e32 vcc, s92, v4
	s_cbranch_vccz .Lrx23_102
	v_bfe_u32 v5, v68, s62, 8
	v_cndmask_b32_e64 v4, 0, 1, vcc
	v_lshl_add_u32 v5, v5, 2, v3
	ds_add_u32 v5, v4
.Lrx23_102:
	v_xor_b32_e32 v172, v181, v69
	v_cmp_gt_u32_e32 vcc, s92, v172
	s_cbranch_vccz .Lrx23_103
	v_bfe_u32 v173, v69, s62, 8
	v_cndmask_b32_e64 v172, 0, 1, vcc
	v_lshl_add_u32 v173, v173, 2, v3
	ds_add_u32 v173, v172
.Lrx23_103:
.Lrx_p23_g13:
	s_and_b64 vcc, exec, s[30:31]
	s_cbranch_vccnz .Lrx_p23_g14
	v_xor_b32_e32 v4, v181, v54
	v_cmp_gt_u32_e32 vcc, s92, v4
	s_cbranch_vccz .Lrx23_104
	v_bfe_u32 v5, v54, s62, 8
	v_cndmask_b32_e64 v4, 0, 1, vcc
	v_lshl_add_u32 v5, v5, 2, v3
	ds_add_u32 v5, v4
.Lrx23_104:
	v_xor_b32_e32 v172, v181, v55
	v_cmp_gt_u32_e32 vcc, s92, v172
	s_cbranch_vccz .Lrx23_105
	v_bfe_u32 v173, v55, s62, 8
	v_cndmask_b32_e64 v172, 0, 1, vcc
	v_lshl_add_u32 v173, v173, 2, v3
	ds_add_u32 v173, v172
.Lrx23_105:
	v_xor_b32_e32 v4, v181, v56
	v_cmp_gt_u32_e32 vcc, s92, v4
	s_cbranch_vccz .Lrx23_106
	v_bfe_u32 v5, v56, s62, 8
	v_cndmask_b32_e64 v4, 0, 1, vcc
	v_lshl_add_u32 v5, v5, 2, v3
	ds_add_u32 v5, v4
.Lrx23_106:
	v_xor_b32_e32 v172, v181, v57
	v_cmp_gt_u32_e32 vcc, s92, v172
	s_cbranch_vccz .Lrx23_107
	v_bfe_u32 v173, v57, s62, 8
	v_cndmask_b32_e64 v172, 0, 1, vcc
	v_lshl_add_u32 v173, v173, 2, v3
	ds_add_u32 v173, v172
.Lrx23_107:
	v_xor_b32_e32 v4, v181, v58
	v_cmp_gt_u32_e32 vcc, s92, v4
	s_cbranch_vccz .Lrx23_108
	v_bfe_u32 v5, v58, s62, 8
	v_cndmask_b32_e64 v4, 0, 1, vcc
	v_lshl_add_u32 v5, v5, 2, v3
	ds_add_u32 v5, v4
.Lrx23_108:
	v_xor_b32_e32 v172, v181, v59
	v_cmp_gt_u32_e32 vcc, s92, v172
	s_cbranch_vccz .Lrx23_109
	v_bfe_u32 v173, v59, s62, 8
	v_cndmask_b32_e64 v172, 0, 1, vcc
	v_lshl_add_u32 v173, v173, 2, v3
	ds_add_u32 v173, v172
.Lrx23_109:
	v_xor_b32_e32 v4, v181, v60
	v_cmp_gt_u32_e32 vcc, s92, v4
	s_cbranch_vccz .Lrx23_110
	v_bfe_u32 v5, v60, s62, 8
	v_cndmask_b32_e64 v4, 0, 1, vcc
	v_lshl_add_u32 v5, v5, 2, v3
	ds_add_u32 v5, v4
.Lrx23_110:
	v_xor_b32_e32 v172, v181, v61
	v_cmp_gt_u32_e32 vcc, s92, v172
	s_cbranch_vccz .Lrx23_111
	v_bfe_u32 v173, v61, s62, 8
	v_cndmask_b32_e64 v172, 0, 1, vcc
	v_lshl_add_u32 v173, v173, 2, v3
	ds_add_u32 v173, v172
.Lrx23_111:
.Lrx_p23_g14:
	s_and_b64 vcc, exec, s[30:31]
	s_cbranch_vccnz .Lrx_p23_g15
	v_xor_b32_e32 v4, v181, v26
	v_cmp_gt_u32_e32 vcc, s92, v4
	s_cbranch_vccz .Lrx23_112
	v_bfe_u32 v5, v26, s62, 8
	v_cndmask_b32_e64 v4, 0, 1, vcc
	v_lshl_add_u32 v5, v5, 2, v3
	ds_add_u32 v5, v4
.Lrx23_112:
	v_xor_b32_e32 v172, v181, v23
	v_cmp_gt_u32_e32 vcc, s92, v172
	s_cbranch_vccz .Lrx23_113
	v_bfe_u32 v173, v23, s62, 8
	v_cndmask_b32_e64 v172, 0, 1, vcc
	v_lshl_add_u32 v173, v173, 2, v3
	ds_add_u32 v173, v172
.Lrx23_113:
	v_xor_b32_e32 v4, v181, v25
	v_cmp_gt_u32_e32 vcc, s92, v4
	s_cbranch_vccz .Lrx23_114
	v_bfe_u32 v5, v25, s62, 8
	v_cndmask_b32_e64 v4, 0, 1, vcc
	v_lshl_add_u32 v5, v5, 2, v3
	ds_add_u32 v5, v4
.Lrx23_114:
	v_xor_b32_e32 v172, v181, v21
	v_cmp_gt_u32_e32 vcc, s92, v172
	s_cbranch_vccz .Lrx23_115
	v_bfe_u32 v173, v21, s62, 8
	v_cndmask_b32_e64 v172, 0, 1, vcc
	v_lshl_add_u32 v173, v173, 2, v3
	ds_add_u32 v173, v172
.Lrx23_115:
	v_xor_b32_e32 v4, v181, v22
	v_cmp_gt_u32_e32 vcc, s92, v4
	s_cbranch_vccz .Lrx23_116
	v_bfe_u32 v5, v22, s62, 8
	v_cndmask_b32_e64 v4, 0, 1, vcc
	v_lshl_add_u32 v5, v5, 2, v3
	ds_add_u32 v5, v4
.Lrx23_116:
	v_xor_b32_e32 v172, v181, v24
	v_cmp_gt_u32_e32 vcc, s92, v172
	s_cbranch_vccz .Lrx23_117
	v_bfe_u32 v173, v24, s62, 8
	v_cndmask_b32_e64 v172, 0, 1, vcc
	v_lshl_add_u32 v173, v173, 2, v3
	ds_add_u32 v173, v172
; __global__ void __launch_bounds__(NWAVES * 64, 2) mega_fwd(Args args) {
;     ...
; #pragma unroll
;                 for (int ti = 0; ti < 4; ++ti)
; #pragma unroll
;                     for (int e = 0; e < 32; ++e) { const unsigned k = keys[ti][e];
;                         const unsigned x = ((k >> pshift) ^ prefix) & pmask; const unsigned inc = 1u - __builtin_elementwise_min(x, 1u);
;                         if (F.wave + 8 * ti < ntiles) __hip_atomic_fetch_add(hist + r32 * HSTR + ((k >> shift) & 255u), inc, __ATOMIC_RELAXED, __HIP_MEMORY_SCOPE_WORKGROUP);
;                         if ((e & 7) == 7) __builtin_amdgcn_sched_barrier(0); }
.Lrx23_117:
	v_xor_b32_e32 v4, v181, v20
	v_cmp_gt_u32_e32 vcc, s92, v4
	s_cbranch_vccz .Lrx23_118
	v_bfe_u32 v5, v20, s62, 8
	v_cndmask_b32_e64 v4, 0, 1, vcc
	v_lshl_add_u32 v5, v5, 2, v3
	ds_add_u32 v5, v4
.Lrx23_118:
	v_xor_b32_e32 v172, v181, v18
	v_cmp_gt_u32_e32 vcc, s92, v172
	s_cbranch_vccz .Lrx23_119
	v_bfe_u32 v173, v18, s62, 8
	v_cndmask_b32_e64 v172, 0, 1, vcc
	v_lshl_add_u32 v173, v173, 2, v3
	ds_add_u32 v173, v172
.Lrx23_119:
.Lrx_p23_g15:
	s_and_b64 vcc, exec, s[30:31]
	s_cbranch_vccnz .Lrx_p23_g16
	v_xor_b32_e32 v4, v181, v19
	v_cmp_gt_u32_e32 vcc, s92, v4
	s_cbranch_vccz .Lrx23_120
	v_bfe_u32 v5, v19, s62, 8
	v_cndmask_b32_e64 v4, 0, 1, vcc
	v_lshl_add_u32 v5, v5, 2, v3
	ds_add_u32 v5, v4
.Lrx23_120:
	v_xor_b32_e32 v172, v181, v11
	v_cmp_gt_u32_e32 vcc, s92, v172
	s_cbranch_vccz .Lrx23_121
	v_bfe_u32 v173, v11, s62, 8
	v_cndmask_b32_e64 v172, 0, 1, vcc
	v_lshl_add_u32 v173, v173, 2, v3
	ds_add_u32 v173, v172
.Lrx23_121:
	v_xor_b32_e32 v4, v181, v9
	v_cmp_gt_u32_e32 vcc, s92, v4
	s_cbranch_vccz .Lrx23_122
	v_bfe_u32 v5, v9, s62, 8
	v_cndmask_b32_e64 v4, 0, 1, vcc
	v_lshl_add_u32 v5, v5, 2, v3
	ds_add_u32 v5, v4
.Lrx23_122:
	v_xor_b32_e32 v172, v181, v13
	v_cmp_gt_u32_e32 vcc, s92, v172
	s_cbranch_vccz .Lrx23_123
	v_bfe_u32 v173, v13, s62, 8
	v_cndmask_b32_e64 v172, 0, 1, vcc
	v_lshl_add_u32 v173, v173, 2, v3
	ds_add_u32 v173, v172
.Lrx23_123:
	v_xor_b32_e32 v4, v181, v12
	v_cmp_gt_u32_e32 vcc, s92, v4
	s_cbranch_vccz .Lrx23_124
	v_bfe_u32 v5, v12, s62, 8
	v_cndmask_b32_e64 v4, 0, 1, vcc
	v_lshl_add_u32 v5, v5, 2, v3
	ds_add_u32 v5, v4
.Lrx23_124:
	v_xor_b32_e32 v172, v181, v10
	v_cmp_gt_u32_e32 vcc, s92, v172
	s_cbranch_vccz .Lrx23_125
	v_bfe_u32 v173, v10, s62, 8
	v_cndmask_b32_e64 v172, 0, 1, vcc
	v_lshl_add_u32 v173, v173, 2, v3
	ds_add_u32 v173, v172
.Lrx23_125:
	v_xor_b32_e32 v4, v181, v8
	v_cmp_gt_u32_e32 vcc, s92, v4
	s_cbranch_vccz .Lrx23_126
	v_bfe_u32 v5, v8, s62, 8
	v_cndmask_b32_e64 v4, 0, 1, vcc
	v_lshl_add_u32 v5, v5, 2, v3
	ds_add_u32 v5, v4
.Lrx23_126:
	v_xor_b32_e32 v172, v181, v2
	v_cmp_gt_u32_e32 vcc, s92, v172
	s_cbranch_vccz .Lrx23_127
	v_bfe_u32 v173, v2, s62, 8
	v_cndmask_b32_e64 v172, 0, 1, vcc
	v_lshl_add_u32 v173, v173, 2, v3
	ds_add_u32 v173, v172
.Lrx23_127:
.Lrx_p23_g16:
	s_branch .LBB0_699
.Lrx_generic2:
	s_and_b64 vcc, exec, s[38:39]
	s_cbranch_vccnz .LBB0_669
	v_lshrrev_b32_e32 v4, s63, v115
	s_waitcnt lgkmcnt(0)
	v_cmp_eq_u32_e32 vcc, v4, v15
	s_or_b64 s[76:77], s[54:55], vcc
	v_bfe_u32 v5, v115, s62, 8
	v_cndmask_b32_e64 v4, 0, 1, s[76:77]
	v_lshl_add_u32 v5, v5, 2, v3
	ds_add_u32 v5, v4
	v_lshrrev_b32_e32 v4, s63, v116
	v_cmp_eq_u32_e32 vcc, v4, v15
	s_or_b64 s[76:77], s[54:55], vcc
	v_bfe_u32 v5, v116, s62, 8
	v_cndmask_b32_e64 v4, 0, 1, s[76:77]
	v_lshl_add_u32 v5, v5, 2, v3
	ds_add_u32 v5, v4
	v_lshrrev_b32_e32 v4, s63, v114
	v_cmp_eq_u32_e32 vcc, v4, v15
	s_or_b64 s[76:77], s[54:55], vcc
	v_bfe_u32 v5, v114, s62, 8
	v_cndmask_b32_e64 v4, 0, 1, s[76:77]
	v_lshl_add_u32 v5, v5, 2, v3
	ds_add_u32 v5, v4
	v_lshrrev_b32_e32 v4, s63, v117
	v_cmp_eq_u32_e32 vcc, v4, v15
	s_or_b64 s[76:77], s[54:55], vcc
	v_bfe_u32 v5, v117, s62, 8
	v_cndmask_b32_e64 v4, 0, 1, s[76:77]
	v_lshl_add_u32 v5, v5, 2, v3
	ds_add_u32 v5, v4
	v_lshrrev_b32_e32 v4, s63, v50
	v_cmp_eq_u32_e32 vcc, v4, v15
	s_or_b64 s[76:77], s[54:55], vcc
	v_bfe_u32 v5, v50, s62, 8
	v_cndmask_b32_e64 v4, 0, 1, s[76:77]
	v_lshl_add_u32 v5, v5, 2, v3
	ds_add_u32 v5, v4
	v_lshrrev_b32_e32 v4, s63, v51
	v_cmp_eq_u32_e32 vcc, v4, v15
	s_or_b64 s[76:77], s[54:55], vcc
	v_bfe_u32 v5, v51, s62, 8
	v_cndmask_b32_e64 v4, 0, 1, s[76:77]
	v_lshl_add_u32 v5, v5, 2, v3
	ds_add_u32 v5, v4
	v_lshrrev_b32_e32 v4, s63, v52
	v_cmp_eq_u32_e32 vcc, v4, v15
	s_or_b64 s[76:77], s[54:55], vcc
	v_bfe_u32 v5, v52, s62, 8
	v_cndmask_b32_e64 v4, 0, 1, s[76:77]
	v_lshl_add_u32 v5, v5, 2, v3
	ds_add_u32 v5, v4
	v_lshrrev_b32_e32 v4, s63, v53
	v_cmp_eq_u32_e32 vcc, v4, v15
	s_or_b64 s[76:77], s[54:55], vcc
	v_bfe_u32 v5, v53, s62, 8
	v_cndmask_b32_e64 v4, 0, 1, s[76:77]
	v_lshl_add_u32 v5, v5, 2, v3
	ds_add_u32 v5, v4
